# baseline (speedup 1.0000x reference)
_Z11prep_kernelPKfS0_S0_S0_S0_S0_S0_S0_S0_PKiPDv8_DF16bS4_PfS5_S5_PiPt:
	s_load_dwordx4 s[16:19], s[0:1], 0x0
	s_load_dwordx4 s[20:23], s[0:1], 0x10
	s_load_dwordx4 s[24:27], s[0:1], 0x20
	s_load_dwordx4 s[28:31], s[0:1], 0x30
	s_load_dwordx4 s[32:35], s[0:1], 0x40
	s_load_dwordx2 s[36:37], s[0:1], 0x80
	v_and_b32_e32 v126, 63, v0
	v_lshrrev_b32_e32 v128, 6, v0
	v_and_b32_e32 v1, 15, v0
	v_bfe_u32 v24, v0, 4, 2
	v_lshl_or_b32 v107, v128, 4, v1
	v_lshlrev_b32_e32 v106, 2, v107
	v_lshlrev_b32_e32 v127, 2, v0
	v_lshlrev_b32_e32 v25, 1, v107
	v_and_b32_e32 v26, 48, v0
	v_mul_u32_u24_e32 v27, 0x440, v24
	v_lshlrev_b32_e32 v232, 4, v0
	v_lshrrev_b32_e32 v58, 5, v0
	v_mul_u32_u24_e32 v58, 0x110, v58
	v_and_b32_e32 v239, 31, v0
	v_lshl_add_u32 v58, v239, 3, v58
	v_add_u32_e32 v238, 0x1b400, v58
	v_mul_u32_u24_e32 v52, 0x110, v1
	v_add_u32_e32 v52, v52, v26
	v_add_u32_e32 v53, 0x1b400, v52
	v_add_u32_e32 v54, 0x1c500, v52
	v_add_u32_e32 v55, v27, v25
	v_add_u32_e32 v55, 0x1c500, v55
	v_mul_u32_u24_e32 v56, 0x110, v107
	v_add_u32_e32 v56, v56, v26
	v_add_u32_e32 v57, 0x8800, v56
	s_lshl_b32 s12, s2, 4
	s_add_i32 s3, s12, 0xfffff800
	s_cmpk_gt_i32 s2, 0x7f
	s_cselect_b64 s[6:7], -1, 0
	s_mov_b32 s48, 0
	s_mov_b32 s49, -1
	v_lshl_or_b32 v236, s2, 3, v128
	v_lshlrev_b32_e32 v236, 12, v236
	v_lshl_add_u32 v236, v126, 4, v236
	s_waitcnt lgkmcnt(0)
	s_cmpk_lt_i32 s2, 0x80
	s_cselect_b32 s38, s16, s18
	s_cselect_b32 s39, s17, s19
	s_cselect_b32 s40, s20, s24
	s_cselect_b32 s41, s21, s25
	s_cselect_b32 s13, s12, s3
	s_cselect_b32 s44, 0x3db504f3, 1.0
	s_lshl_b32 s13, s13, 9
	s_add_u32 s38, s38, s13
	s_addc_u32 s39, s39, 0
	global_load_dwordx4 v[2:5], v232, s[38:39] nt
	s_and_b32 s13, s2, 7
	s_lshl_b32 s14, s13, 13
	v_add_u32_e32 v239, s14, v232
	global_load_dwordx4 v[132:135], v239, s[40:41]
	s_add_i32 s13, s2, 1
	s_and_b32 s13, s13, 7
	s_lshl_b32 s14, s13, 13
	v_add_u32_e32 v239, s14, v232
	global_load_dwordx4 v[136:139], v239, s[40:41]
	s_add_i32 s13, s2, 2
	s_and_b32 s13, s13, 7
	s_lshl_b32 s14, s13, 13
	v_add_u32_e32 v239, s14, v232
	global_load_dwordx4 v[140:143], v239, s[40:41]
	s_add_i32 s13, s2, 3
	s_and_b32 s13, s13, 7
	s_lshl_b32 s14, s13, 13
	v_add_u32_e32 v239, s14, v232
	global_load_dwordx4 v[144:147], v239, s[40:41]
	s_add_i32 s13, s2, 4
	s_and_b32 s13, s13, 7
	s_lshl_b32 s14, s13, 13
	v_add_u32_e32 v239, s14, v232
	global_load_dwordx4 v[148:151], v239, s[40:41]
	s_add_i32 s13, s2, 5
	s_and_b32 s13, s13, 7
	s_lshl_b32 s14, s13, 13
	v_add_u32_e32 v239, s14, v232
	global_load_dwordx4 v[152:155], v239, s[40:41]
	s_add_i32 s13, s2, 6
	s_and_b32 s13, s13, 7
	s_lshl_b32 s14, s13, 13
	v_add_u32_e32 v239, s14, v232
	global_load_dwordx4 v[156:159], v239, s[40:41]
	s_add_i32 s13, s2, 7
	s_and_b32 s13, s13, 7
	s_lshl_b32 s14, s13, 13
	v_add_u32_e32 v239, s14, v232
	global_load_dwordx4 v[160:163], v239, s[40:41]
	global_load_dword v129, v106, s[32:33]
	global_load_dword v130, v106, s[30:31]
	s_and_b64 vcc, exec, s[6:7]
	s_cbranch_vccz .Lp_q
	v_cmp_gt_u32_e32 vcc, 32, v126
	v_mov_b32_e32 v244, 0x3db504f3
	v_mov_b32_e32 v239, s22
	v_mov_b32_e32 v240, s26
	v_cndmask_b32_e32 v244, 1.0, v244, vcc
	v_cndmask_b32_e32 v240, v240, v239, vcc
	v_mov_b32_e32 v239, s23
	v_mov_b32_e32 v241, s27
	v_cndmask_b32_e32 v241, v241, v239, vcc
	v_and_b32_e32 v242, 31, v126
	v_lshlrev_b32_e32 v242, 4, v242
	v_mov_b32_e32 v243, 0
	v_lshl_add_u64 v[240:241], v[240:241], 0, v[242:243]
	global_load_dwordx4 v[228:231], v[240:241], off
	v_lshlrev_b32_e32 v233, 14, v128
	v_lshl_add_u32 v233, v126, 4, v233
	s_and_b32 s13, s2, 15
	s_lshl_b32 s14, s13, 10
	s_add_u32 s46, s28, s14
	s_addc_u32 s47, s29, 0
	global_load_dwordx4 v[164:167], v233, s[46:47]
	s_add_i32 s13, s2, 1
	s_and_b32 s13, s13, 15
	s_lshl_b32 s14, s13, 10
	s_add_u32 s46, s28, s14
	s_addc_u32 s47, s29, 0
	global_load_dwordx4 v[168:171], v233, s[46:47]
	s_add_i32 s13, s2, 2
	s_and_b32 s13, s13, 15
	s_lshl_b32 s14, s13, 10
	s_add_u32 s46, s28, s14
	s_addc_u32 s47, s29, 0
	global_load_dwordx4 v[172:175], v233, s[46:47]
	s_add_i32 s13, s2, 3
	s_and_b32 s13, s13, 15
	s_lshl_b32 s14, s13, 10
	s_add_u32 s46, s28, s14
	s_addc_u32 s47, s29, 0
	global_load_dwordx4 v[176:179], v233, s[46:47]
	s_add_i32 s13, s2, 4
	s_and_b32 s13, s13, 15
	s_lshl_b32 s14, s13, 10
	s_add_u32 s46, s28, s14
	s_addc_u32 s47, s29, 0
	global_load_dwordx4 v[180:183], v233, s[46:47]
	s_add_i32 s13, s2, 5
	s_and_b32 s13, s13, 15
	s_lshl_b32 s14, s13, 10
	s_add_u32 s46, s28, s14
	s_addc_u32 s47, s29, 0
	global_load_dwordx4 v[184:187], v233, s[46:47]
	s_add_i32 s13, s2, 6
	s_and_b32 s13, s13, 15
	s_lshl_b32 s14, s13, 10
	s_add_u32 s46, s28, s14
	s_addc_u32 s47, s29, 0
	global_load_dwordx4 v[188:191], v233, s[46:47]
	s_add_i32 s13, s2, 7
	s_and_b32 s13, s13, 15
	s_lshl_b32 s14, s13, 10
	s_add_u32 s46, s28, s14
	s_addc_u32 s47, s29, 0
	global_load_dwordx4 v[192:195], v233, s[46:47]
	s_add_i32 s13, s2, 8
	s_and_b32 s13, s13, 15
	s_lshl_b32 s14, s13, 10
	s_add_u32 s46, s28, s14
	s_addc_u32 s47, s29, 0
	global_load_dwordx4 v[196:199], v233, s[46:47]
	s_add_i32 s13, s2, 9
	s_and_b32 s13, s13, 15
	s_lshl_b32 s14, s13, 10
	s_add_u32 s46, s28, s14
	s_addc_u32 s47, s29, 0
	global_load_dwordx4 v[200:203], v233, s[46:47]
	s_add_i32 s13, s2, 10
	s_and_b32 s13, s13, 15
	s_lshl_b32 s14, s13, 10
	s_add_u32 s46, s28, s14
	s_addc_u32 s47, s29, 0
	global_load_dwordx4 v[204:207], v233, s[46:47]
	s_add_i32 s13, s2, 11
	s_and_b32 s13, s13, 15
	s_lshl_b32 s14, s13, 10
	s_add_u32 s46, s28, s14
	s_addc_u32 s47, s29, 0
	global_load_dwordx4 v[208:211], v233, s[46:47]
	s_add_i32 s13, s2, 12
	s_and_b32 s13, s13, 15
	s_lshl_b32 s14, s13, 10
	s_add_u32 s46, s28, s14
	s_addc_u32 s47, s29, 0
	global_load_dwordx4 v[212:215], v233, s[46:47]
	s_add_i32 s13, s2, 13
	s_and_b32 s13, s13, 15
	s_lshl_b32 s14, s13, 10
	s_add_u32 s46, s28, s14
	s_addc_u32 s47, s29, 0
	global_load_dwordx4 v[216:219], v233, s[46:47]
	s_add_i32 s13, s2, 14
	s_and_b32 s13, s13, 15
	s_lshl_b32 s14, s13, 10
	s_add_u32 s46, s28, s14
	s_addc_u32 s47, s29, 0
	global_load_dwordx4 v[220:223], v233, s[46:47]
	s_add_i32 s13, s2, 15
	s_and_b32 s13, s13, 15
	s_lshl_b32 s14, s13, 10
	s_add_u32 s46, s28, s14
	s_addc_u32 s47, s29, 0
	global_load_dwordx4 v[224:227], v233, s[46:47]
	v_mul_u32_u24_e32 v59, 0x1040, v128
	v_lshl_add_u32 v59, v126, 2, v59
	v_add_u32_e32 v59, 0x11000, v59
	v_mul_u32_u24_e32 v76, 0x1100, v128
	v_lshl_add_u32 v76, v126, 3, v76
	v_add_u32_e32 v76, 0x8700, v76
	v_lshrrev_b32_e32 v77, 2, v126
	v_mul_u32_u24_e32 v77, 0x104, v77
	v_mul_u32_u24_e32 v239, 0x1040, v128
	v_add_u32_e32 v77, v77, v239
	v_and_b32_e32 v239, 3, v126
	v_lshl_add_u32 v77, v239, 6, v77
	v_add_u32_e32 v77, 0x11000, v77
	s_waitcnt vmcnt(27)
	v_cvt_pk_bf16_f32 v12, v2, v3
	v_cvt_pk_bf16_f32 v13, v4, v5
	ds_write_b64 v238, v[12:13]
	s_waitcnt vmcnt(26)
	v_cvt_pk_bf16_f32 v6, v132, v133
	v_cvt_pk_bf16_f32 v7, v134, v135
	s_and_b32 s13, s2, 7
	s_mul_i32 s14, s13, 0x1100
	v_add_u32_e32 v239, s14, v58
	ds_write_b64 v239, v[6:7]
	s_waitcnt vmcnt(25)
	v_cvt_pk_bf16_f32 v8, v136, v137
	v_cvt_pk_bf16_f32 v9, v138, v139
	s_add_i32 s13, s2, 1
	s_and_b32 s13, s13, 7
	s_mul_i32 s14, s13, 0x1100
	v_add_u32_e32 v10, s14, v58
	ds_write_b64 v10, v[8:9]
	s_waitcnt vmcnt(24)
	v_cvt_pk_bf16_f32 v6, v140, v141
	v_cvt_pk_bf16_f32 v7, v142, v143
	s_add_i32 s13, s2, 2
	s_and_b32 s13, s13, 7
	s_mul_i32 s14, s13, 0x1100
	v_add_u32_e32 v239, s14, v58
	ds_write_b64 v239, v[6:7]
	s_waitcnt vmcnt(23)
	v_cvt_pk_bf16_f32 v8, v144, v145
	v_cvt_pk_bf16_f32 v9, v146, v147
	s_add_i32 s13, s2, 3
	s_and_b32 s13, s13, 7
	s_mul_i32 s14, s13, 0x1100
	v_add_u32_e32 v10, s14, v58
	ds_write_b64 v10, v[8:9]
	s_waitcnt vmcnt(22)
	v_cvt_pk_bf16_f32 v6, v148, v149
	v_cvt_pk_bf16_f32 v7, v150, v151
	s_add_i32 s13, s2, 4
	s_and_b32 s13, s13, 7
	s_mul_i32 s14, s13, 0x1100
	v_add_u32_e32 v239, s14, v58
	ds_write_b64 v239, v[6:7]
	s_waitcnt vmcnt(21)
	v_cvt_pk_bf16_f32 v8, v152, v153
	v_cvt_pk_bf16_f32 v9, v154, v155
	s_add_i32 s13, s2, 5
	s_and_b32 s13, s13, 7
	s_mul_i32 s14, s13, 0x1100
	v_add_u32_e32 v10, s14, v58
	ds_write_b64 v10, v[8:9]
	s_waitcnt vmcnt(20)
	v_cvt_pk_bf16_f32 v6, v156, v157
	v_cvt_pk_bf16_f32 v7, v158, v159
	s_add_i32 s13, s2, 6
	s_and_b32 s13, s13, 7
	s_mul_i32 s14, s13, 0x1100
	v_add_u32_e32 v239, s14, v58
	ds_write_b64 v239, v[6:7]
	s_waitcnt vmcnt(19)
	v_cvt_pk_bf16_f32 v8, v160, v161
	v_cvt_pk_bf16_f32 v9, v162, v163
	s_add_i32 s13, s2, 7
	s_and_b32 s13, s13, 7
	s_mul_i32 s14, s13, 0x1100
	v_add_u32_e32 v10, s14, v58
	ds_write_b64 v10, v[8:9]
	s_waitcnt lgkmcnt(0)
	s_barrier
	ds_read_b128 v[28:31], v53
	ds_read_b128 v[60:63], v56
	ds_read_b128 v[32:35], v53 offset:64
	ds_read_b128 v[64:67], v56 offset:64
	ds_read_b128 v[36:39], v53 offset:128
	ds_read_b128 v[68:71], v56 offset:128
	ds_read_b128 v[40:43], v53 offset:192
	ds_read_b128 v[72:75], v56 offset:192
	s_waitcnt lgkmcnt(6)
	v_mfma_f32_16x16x32_bf16 v[18:21], v[28:31], v[60:63], 0
	s_waitcnt lgkmcnt(4)
	v_mfma_f32_16x16x32_bf16 v[18:21], v[32:35], v[64:67], v[18:21]
	s_waitcnt lgkmcnt(2)
	v_mfma_f32_16x16x32_bf16 v[18:21], v[36:39], v[68:71], v[18:21]
	s_waitcnt lgkmcnt(0)
	v_mfma_f32_16x16x32_bf16 v[18:21], v[40:43], v[72:75], v[18:21]
	s_nop 7
	v_mul_f32_e32 v18, s44, v18
	v_mul_f32_e32 v19, s44, v19
	v_mul_f32_e32 v20, s44, v20
	v_mul_f32_e32 v21, s44, v21
	v_cvt_pk_bf16_f32 v18, v18, v18
	v_cvt_pk_bf16_f32 v19, v19, v19
	v_cvt_pk_bf16_f32 v20, v20, v20
	v_cvt_pk_bf16_f32 v21, v21, v21
	ds_write_b16 v55, v18
	ds_write_b16 v55, v19 offset:272
	ds_write_b16 v55, v20 offset:544
	ds_write_b16 v55, v21 offset:816
	s_waitcnt vmcnt(16)
	v_pk_mul_f32 v[228:229], v[244:245], v[228:229] op_sel_hi:[0,1]
	v_pk_mul_f32 v[230:231], v[244:245], v[230:231] op_sel_hi:[0,1]
	s_waitcnt vmcnt(15)
	v_mul_f32_e32 v6, v229, v165
	v_mul_f32_e32 v7, v231, v167
	v_fmac_f32_e32 v6, v228, v164
	v_fmac_f32_e32 v7, v230, v166
	s_and_b32 s13, s2, 15
	s_mul_i32 s14, s13, 0x104
	s_mul_i32 s15, s13, 0x110
	v_add_f32_e32 v6, v6, v7
	v_add_u32_e32 v239, s14, v59
	ds_write_b32 v239, v6
	v_cvt_pk_bf16_f32 v8, v164, v165
	v_cvt_pk_bf16_f32 v9, v166, v167
	v_add_u32_e32 v10, s15, v76
	s_mov_b64 exec, s[48:49]
	ds_write_b64 v10, v[8:9]
	s_mov_b64 exec, -1
	s_waitcnt vmcnt(14)
	v_mul_f32_e32 v11, v229, v169
	v_mul_f32_e32 v15, v231, v171
	v_fmac_f32_e32 v11, v228, v168
	v_fmac_f32_e32 v15, v230, v170
	s_add_i32 s13, s2, 1
	s_and_b32 s13, s13, 15
	s_mul_i32 s14, s13, 0x104
	s_mul_i32 s15, s13, 0x110
	v_add_f32_e32 v11, v11, v15
	v_add_u32_e32 v16, s14, v59
	ds_write_b32 v16, v11
	v_cvt_pk_bf16_f32 v12, v168, v169
	v_cvt_pk_bf16_f32 v13, v170, v171
	v_add_u32_e32 v14, s15, v76
	s_mov_b64 exec, s[48:49]
	ds_write_b64 v14, v[12:13]
	s_mov_b64 exec, -1
	s_waitcnt vmcnt(13)
	v_mul_f32_e32 v6, v229, v173
	v_mul_f32_e32 v7, v231, v175
	v_fmac_f32_e32 v6, v228, v172
	v_fmac_f32_e32 v7, v230, v174
	s_add_i32 s13, s2, 2
	s_and_b32 s13, s13, 15
	s_mul_i32 s14, s13, 0x104
	s_mul_i32 s15, s13, 0x110
	v_add_f32_e32 v6, v6, v7
	v_add_u32_e32 v239, s14, v59
	ds_write_b32 v239, v6
	v_cvt_pk_bf16_f32 v8, v172, v173
	v_cvt_pk_bf16_f32 v9, v174, v175
	v_add_u32_e32 v10, s15, v76
	s_mov_b64 exec, s[48:49]
	ds_write_b64 v10, v[8:9]
	s_mov_b64 exec, -1
	s_waitcnt vmcnt(12)
	v_mul_f32_e32 v11, v229, v177
	v_mul_f32_e32 v15, v231, v179
	v_fmac_f32_e32 v11, v228, v176
	v_fmac_f32_e32 v15, v230, v178
	s_add_i32 s13, s2, 3
	s_and_b32 s13, s13, 15
	s_mul_i32 s14, s13, 0x104
	s_mul_i32 s15, s13, 0x110
	v_add_f32_e32 v11, v11, v15
	v_add_u32_e32 v16, s14, v59
	ds_write_b32 v16, v11
	v_cvt_pk_bf16_f32 v12, v176, v177
	v_cvt_pk_bf16_f32 v13, v178, v179
	v_add_u32_e32 v14, s15, v76
	s_mov_b64 exec, s[48:49]
	ds_write_b64 v14, v[12:13]
	s_mov_b64 exec, -1
	s_waitcnt vmcnt(11)
	v_mul_f32_e32 v6, v229, v181
	v_mul_f32_e32 v7, v231, v183
	v_fmac_f32_e32 v6, v228, v180
	v_fmac_f32_e32 v7, v230, v182
	s_add_i32 s13, s2, 4
	s_and_b32 s13, s13, 15
	s_mul_i32 s14, s13, 0x104
	s_mul_i32 s15, s13, 0x110
	v_add_f32_e32 v6, v6, v7
	v_add_u32_e32 v239, s14, v59
	ds_write_b32 v239, v6
	v_cvt_pk_bf16_f32 v8, v180, v181
	v_cvt_pk_bf16_f32 v9, v182, v183
	v_add_u32_e32 v10, s15, v76
	s_mov_b64 exec, s[48:49]
	ds_write_b64 v10, v[8:9]
	s_mov_b64 exec, -1
	s_waitcnt vmcnt(10)
	v_mul_f32_e32 v11, v229, v185
	v_mul_f32_e32 v15, v231, v187
	v_fmac_f32_e32 v11, v228, v184
	v_fmac_f32_e32 v15, v230, v186
	s_add_i32 s13, s2, 5
	s_and_b32 s13, s13, 15
	s_mul_i32 s14, s13, 0x104
	s_mul_i32 s15, s13, 0x110
	v_add_f32_e32 v11, v11, v15
	v_add_u32_e32 v16, s14, v59
	ds_write_b32 v16, v11
	v_cvt_pk_bf16_f32 v12, v184, v185
	v_cvt_pk_bf16_f32 v13, v186, v187
	v_add_u32_e32 v14, s15, v76
	s_mov_b64 exec, s[48:49]
	ds_write_b64 v14, v[12:13]
	s_mov_b64 exec, -1
	s_waitcnt vmcnt(9)
	v_mul_f32_e32 v6, v229, v189
	v_mul_f32_e32 v7, v231, v191
	v_fmac_f32_e32 v6, v228, v188
	v_fmac_f32_e32 v7, v230, v190
	s_add_i32 s13, s2, 6
	s_and_b32 s13, s13, 15
	s_mul_i32 s14, s13, 0x104
	s_mul_i32 s15, s13, 0x110
	v_add_f32_e32 v6, v6, v7
	v_add_u32_e32 v239, s14, v59
	ds_write_b32 v239, v6
	v_cvt_pk_bf16_f32 v8, v188, v189
	v_cvt_pk_bf16_f32 v9, v190, v191
	v_add_u32_e32 v10, s15, v76
	s_mov_b64 exec, s[48:49]
	ds_write_b64 v10, v[8:9]
	s_mov_b64 exec, -1
	s_waitcnt vmcnt(8)
	v_mul_f32_e32 v11, v229, v193
	v_mul_f32_e32 v15, v231, v195
	v_fmac_f32_e32 v11, v228, v192
	v_fmac_f32_e32 v15, v230, v194
	s_add_i32 s13, s2, 7
	s_and_b32 s13, s13, 15
	s_mul_i32 s14, s13, 0x104
	s_mul_i32 s15, s13, 0x110
	v_add_f32_e32 v11, v11, v15
	v_add_u32_e32 v16, s14, v59
	ds_write_b32 v16, v11
	v_cvt_pk_bf16_f32 v12, v192, v193
	v_cvt_pk_bf16_f32 v13, v194, v195
	v_add_u32_e32 v14, s15, v76
	s_mov_b64 exec, s[48:49]
	ds_write_b64 v14, v[12:13]
	s_mov_b64 exec, -1
	s_waitcnt vmcnt(7)
	v_mul_f32_e32 v6, v229, v197
	v_mul_f32_e32 v7, v231, v199
	v_fmac_f32_e32 v6, v228, v196
	v_fmac_f32_e32 v7, v230, v198
	s_add_i32 s13, s2, 8
	s_and_b32 s13, s13, 15
	s_mul_i32 s14, s13, 0x104
	s_mul_i32 s15, s13, 0x110
	v_add_f32_e32 v6, v6, v7
	v_add_u32_e32 v239, s14, v59
	ds_write_b32 v239, v6
	v_cvt_pk_bf16_f32 v8, v196, v197
	v_cvt_pk_bf16_f32 v9, v198, v199
	v_add_u32_e32 v10, s15, v76
	s_mov_b64 exec, s[48:49]
	ds_write_b64 v10, v[8:9]
	s_mov_b64 exec, -1
	s_waitcnt vmcnt(6)
	v_mul_f32_e32 v11, v229, v201
	v_mul_f32_e32 v15, v231, v203
	v_fmac_f32_e32 v11, v228, v200
	v_fmac_f32_e32 v15, v230, v202
	s_add_i32 s13, s2, 9
	s_and_b32 s13, s13, 15
	s_mul_i32 s14, s13, 0x104
	s_mul_i32 s15, s13, 0x110
	v_add_f32_e32 v11, v11, v15
	v_add_u32_e32 v16, s14, v59
	ds_write_b32 v16, v11
	v_cvt_pk_bf16_f32 v12, v200, v201
	v_cvt_pk_bf16_f32 v13, v202, v203
	v_add_u32_e32 v14, s15, v76
	s_mov_b64 exec, s[48:49]
	ds_write_b64 v14, v[12:13]
	s_mov_b64 exec, -1
	s_waitcnt vmcnt(5)
	v_mul_f32_e32 v6, v229, v205
	v_mul_f32_e32 v7, v231, v207
	v_fmac_f32_e32 v6, v228, v204
	v_fmac_f32_e32 v7, v230, v206
	s_add_i32 s13, s2, 10
	s_and_b32 s13, s13, 15
	s_mul_i32 s14, s13, 0x104
	s_mul_i32 s15, s13, 0x110
	v_add_f32_e32 v6, v6, v7
	v_add_u32_e32 v239, s14, v59
	ds_write_b32 v239, v6
	v_cvt_pk_bf16_f32 v8, v204, v205
	v_cvt_pk_bf16_f32 v9, v206, v207
	v_add_u32_e32 v10, s15, v76
	s_mov_b64 exec, s[48:49]
	ds_write_b64 v10, v[8:9]
	s_mov_b64 exec, -1
	s_waitcnt vmcnt(4)
	v_mul_f32_e32 v11, v229, v209
	v_mul_f32_e32 v15, v231, v211
	v_fmac_f32_e32 v11, v228, v208
	v_fmac_f32_e32 v15, v230, v210
	s_add_i32 s13, s2, 11
	s_and_b32 s13, s13, 15
	s_mul_i32 s14, s13, 0x104
	s_mul_i32 s15, s13, 0x110
	v_add_f32_e32 v11, v11, v15
	v_add_u32_e32 v16, s14, v59
	ds_write_b32 v16, v11
	v_cvt_pk_bf16_f32 v12, v208, v209
	v_cvt_pk_bf16_f32 v13, v210, v211
	v_add_u32_e32 v14, s15, v76
	s_mov_b64 exec, s[48:49]
	ds_write_b64 v14, v[12:13]
	s_mov_b64 exec, -1
	s_waitcnt vmcnt(3)
	v_mul_f32_e32 v6, v229, v213
	v_mul_f32_e32 v7, v231, v215
	v_fmac_f32_e32 v6, v228, v212
	v_fmac_f32_e32 v7, v230, v214
	s_add_i32 s13, s2, 12
	s_and_b32 s13, s13, 15
	s_mul_i32 s14, s13, 0x104
	s_mul_i32 s15, s13, 0x110
	v_add_f32_e32 v6, v6, v7
	v_add_u32_e32 v239, s14, v59
	ds_write_b32 v239, v6
	v_cvt_pk_bf16_f32 v8, v212, v213
	v_cvt_pk_bf16_f32 v9, v214, v215
	v_add_u32_e32 v10, s15, v76
	s_mov_b64 exec, s[48:49]
	ds_write_b64 v10, v[8:9]
	s_mov_b64 exec, -1
	s_waitcnt vmcnt(2)
	v_mul_f32_e32 v11, v229, v217
	v_mul_f32_e32 v15, v231, v219
	v_fmac_f32_e32 v11, v228, v216
	v_fmac_f32_e32 v15, v230, v218
	s_add_i32 s13, s2, 13
	s_and_b32 s13, s13, 15
	s_mul_i32 s14, s13, 0x104
	s_mul_i32 s15, s13, 0x110
	v_add_f32_e32 v11, v11, v15
	v_add_u32_e32 v16, s14, v59
	ds_write_b32 v16, v11
	v_cvt_pk_bf16_f32 v12, v216, v217
	v_cvt_pk_bf16_f32 v13, v218, v219
	v_add_u32_e32 v14, s15, v76
	s_mov_b64 exec, s[48:49]
	ds_write_b64 v14, v[12:13]
	s_mov_b64 exec, -1
	s_waitcnt vmcnt(1)
	v_mul_f32_e32 v6, v229, v221
	v_mul_f32_e32 v7, v231, v223
	v_fmac_f32_e32 v6, v228, v220
	v_fmac_f32_e32 v7, v230, v222
	s_add_i32 s13, s2, 14
	s_and_b32 s13, s13, 15
	s_mul_i32 s14, s13, 0x104
	s_mul_i32 s15, s13, 0x110
	v_add_f32_e32 v6, v6, v7
	v_add_u32_e32 v239, s14, v59
	ds_write_b32 v239, v6
	v_cvt_pk_bf16_f32 v8, v220, v221
	v_cvt_pk_bf16_f32 v9, v222, v223
	v_add_u32_e32 v10, s15, v76
	s_mov_b64 exec, s[48:49]
	ds_write_b64 v10, v[8:9]
	s_mov_b64 exec, -1
	s_waitcnt vmcnt(0)
	v_mul_f32_e32 v11, v229, v225
	v_mul_f32_e32 v15, v231, v227
	v_fmac_f32_e32 v11, v228, v224
	v_fmac_f32_e32 v15, v230, v226
	s_add_i32 s13, s2, 15
	s_and_b32 s13, s13, 15
	s_mul_i32 s14, s13, 0x104
	s_mul_i32 s15, s13, 0x110
	v_add_f32_e32 v11, v11, v15
	v_add_u32_e32 v16, s14, v59
	ds_write_b32 v16, v11
	v_cvt_pk_bf16_f32 v12, v224, v225
	v_cvt_pk_bf16_f32 v13, v226, v227
	v_add_u32_e32 v14, s15, v76
	s_mov_b64 exec, s[48:49]
	ds_write_b64 v14, v[12:13]
	s_mov_b64 exec, -1
	s_waitcnt lgkmcnt(0)
	ds_read2_b32 v[60:61], v77 offset0:0 offset1:1
	ds_read2_b32 v[62:63], v77 offset0:2 offset1:3
	ds_read2_b32 v[64:65], v77 offset0:4 offset1:5
	ds_read2_b32 v[66:67], v77 offset0:6 offset1:7
	ds_read2_b32 v[68:69], v77 offset0:8 offset1:9
	ds_read2_b32 v[70:71], v77 offset0:10 offset1:11
	ds_read2_b32 v[72:73], v77 offset0:12 offset1:13
	ds_read2_b32 v[74:75], v77 offset0:14 offset1:15
	s_waitcnt lgkmcnt(0)
	v_add_f32_e32 v78, 0, v60
	v_add_f32_e32 v78, v78, v61
	v_add_f32_e32 v78, v78, v62
	v_add_f32_e32 v78, v78, v63
	v_add_f32_e32 v78, v78, v64
	v_add_f32_e32 v78, v78, v65
	v_add_f32_e32 v78, v78, v66
	v_add_f32_e32 v78, v78, v67
	v_add_f32_e32 v78, v78, v68
	v_add_f32_e32 v78, v78, v69
	v_add_f32_e32 v78, v78, v70
	v_add_f32_e32 v78, v78, v71
	v_add_f32_e32 v78, v78, v72
	v_add_f32_e32 v78, v78, v73
	v_add_f32_e32 v78, v78, v74
	v_add_f32_e32 v78, v78, v75
	s_nop 1
	v_add_f32_dpp v78, v78, v78 quad_perm:[1,0,3,2] row_mask:0xf bank_mask:0xf bound_ctrl:1
	s_nop 1
	v_add_f32_dpp v78, v78, v78 quad_perm:[2,3,0,1] row_mask:0xf bank_mask:0xf bound_ctrl:1
	v_lshlrev_b32_e32 v79, 4, v1
	ds_bpermute_b32 v78, v79, v78
	s_waitcnt lgkmcnt(0)
	s_barrier
	global_load_dwordx4 v[2:5], v236, s[34:35] nt
	global_load_dwordx4 v[6:9], v236, s[34:35] offset:1024 nt
	global_load_dwordx4 v[10:13], v236, s[34:35] offset:2048 nt
	global_load_dwordx4 v[14:17], v236, s[34:35] offset:3072 nt
	ds_read_b128 v[28:31], v54
	ds_read_b128 v[60:63], v57
	ds_read_b128 v[32:35], v54 offset:64
	ds_read_b128 v[64:67], v57 offset:64
	ds_read_b128 v[36:39], v54 offset:128
	ds_read_b128 v[68:71], v57 offset:128
	ds_read_b128 v[40:43], v54 offset:192
	ds_read_b128 v[72:75], v57 offset:192
	s_waitcnt lgkmcnt(6)
	v_mfma_f32_16x16x32_bf16 v[18:21], v[28:31], v[60:63], 0
	s_waitcnt lgkmcnt(4)
	v_mfma_f32_16x16x32_bf16 v[18:21], v[32:35], v[64:67], v[18:21]
	s_waitcnt lgkmcnt(2)
	v_mfma_f32_16x16x32_bf16 v[18:21], v[36:39], v[68:71], v[18:21]
	s_waitcnt lgkmcnt(0)
	v_mfma_f32_16x16x32_bf16 v[18:21], v[40:43], v[72:75], v[18:21]
	s_nop 2
	v_mov_b32_e32 v28, v78
	s_load_dwordx2 s[4:5], s[0:1], 0x70
	v_lshl_or_b32 v30, v24, 2, s3
	v_ashrrev_i32_e32 v31, 31, v30
	v_mov_b32_e32 v107, 0
	s_waitcnt lgkmcnt(0)
	v_add_f32_e32 v34, v130, v28
	v_add_f32_e32 v35, v34, v18
	v_add_f32_e32 v28, v35, v35
	v_mul_f32_e32 v28, 0x3fb8aa3b, v28
	v_exp_f32_e32 v32, v28
	v_lshlrev_b64 v[28:29], 9, v[30:31]
	s_mov_b32 s8, 0x19200
	v_add3_u32 v37, v27, v25, s8
	v_add_f32_e32 v31, 1.0, v32
	v_rcp_f32_e32 v31, v31
	v_lshl_add_u64 v[32:33], s[4:5], 0, v[106:107]
	v_lshl_add_u64 v[28:29], v[32:33], 0, v[28:29]
	global_store_dword v[28:29], v35, off sc1
	v_fma_f32 v35, v31, -2.0, 1.0
	v_fma_f32 v28, -v35, v35, 1.0
	v_mul_f32_e32 v28, v129, v28
	v_add_f32_e32 v31, v34, v19
	v_cvt_pk_bf16_f32 v29, v28, s0
	v_mul_f32_e64 v27, v35, -v28
	v_add_f32_e32 v28, v31, v31
	v_mul_f32_e32 v28, 0x3fb8aa3b, v28
	v_exp_f32_e32 v38, v28
	v_cvt_pk_bf16_f32 v27, v27, s0
	ds_write_b16 v37, v27 offset:4352
	v_or_b32_e32 v28, 1, v30
	v_add_f32_e32 v27, 1.0, v38
	v_rcp_f32_e32 v27, v27
	ds_write_b16 v37, v29
	v_ashrrev_i32_e32 v29, 31, v28
	v_lshlrev_b64 v[28:29], 9, v[28:29]
	v_lshl_add_u64 v[28:29], v[32:33], 0, v[28:29]
	v_fma_f32 v27, v27, -2.0, 1.0
	global_store_dword v[28:29], v31, off sc1
	v_fma_f32 v28, -v27, v27, 1.0
	v_mul_f32_e32 v28, v129, v28
	v_cvt_pk_bf16_f32 v29, v28, s0
	v_add_f32_e32 v31, v34, v20
	ds_write_b16 v37, v29 offset:272
	v_add_f32_e32 v29, v31, v31
	v_mul_f32_e32 v29, 0x3fb8aa3b, v29
	v_exp_f32_e32 v38, v29
	v_mul_f32_e64 v28, v27, -v28
	v_cvt_pk_bf16_f32 v28, v28, s0
	ds_write_b16 v37, v28 offset:4624
	v_add_f32_e32 v38, 1.0, v38
	v_or_b32_e32 v28, 2, v30
	v_rcp_f32_e32 v38, v38
	v_ashrrev_i32_e32 v29, 31, v28
	v_lshlrev_b64 v[28:29], 9, v[28:29]
	v_lshl_add_u64 v[28:29], v[32:33], 0, v[28:29]
	global_store_dword v[28:29], v31, off sc1
	v_fma_f32 v28, v38, -2.0, 1.0
	v_fma_f32 v29, -v28, v28, 1.0
	v_mul_f32_e32 v29, v129, v29
	v_cvt_pk_bf16_f32 v31, v29, s0
	v_add_f32_e32 v34, v34, v21
	ds_write_b16 v37, v31 offset:544
	v_add_f32_e32 v31, v34, v34
	v_mul_f32_e32 v31, 0x3fb8aa3b, v31
	v_exp_f32_e32 v38, v31
	v_mul_f32_e64 v29, v28, -v29
	v_cvt_pk_bf16_f32 v29, v29, s0
	ds_write_b16 v37, v29 offset:4896
	v_add_f32_e32 v29, 1.0, v38
	v_rcp_f32_e32 v29, v29
	v_or_b32_e32 v30, 3, v30
	v_ashrrev_i32_e32 v31, 31, v30
	v_lshlrev_b64 v[30:31], 9, v[30:31]
	v_lshl_add_u64 v[30:31], v[32:33], 0, v[30:31]
	v_fma_f32 v29, v29, -2.0, 1.0
	global_store_dword v[30:31], v34, off sc1
	v_fma_f32 v30, -v29, v29, 1.0
	v_mul_f32_e32 v30, v129, v30
	v_cvt_pk_bf16_f32 v31, v30, s0
	v_mul_f32_e64 v30, v29, -v30
	v_cvt_pk_bf16_f32 v30, v30, s0
	ds_write_b16 v37, v30 offset:5168
	v_mov_b32_e32 v30, 0x1d800
	v_mul_f32_e32 v36, v129, v35
	v_lshl_or_b32 v32, v128, 6, v30
	v_mov_b32_e32 v30, v107
	ds_write_b16 v37, v31 offset:816
	v_mov_b32_e32 v31, 0
	v_mov_b32_dpp v30, v36 quad_perm:[1,0,3,2] row_mask:0xf bank_mask:0xf
	v_fmac_f32_e32 v30, v129, v35
	v_cmp_eq_u32_e32 vcc, 0, v1
	v_add_u32_e32 v26, v32, v26
	v_add_f32_dpp v30, v30, v30 quad_perm:[2,3,0,1] row_mask:0xf bank_mask:0xf bound_ctrl:1
	s_nop 1
	v_add_f32_dpp v30, v30, v30 row_half_mirror row_mask:0xf bank_mask:0xf bound_ctrl:1
	s_nop 1
	v_mov_b32_dpp v31, v30 row_mirror row_mask:0xf bank_mask:0xf
	s_and_saveexec_b64 s[4:5], vcc
	v_add_f32_e32 v30, v30, v31
	ds_write_b32 v26, v30
	s_or_b64 exec, exec, s[4:5]
	v_mul_f32_e32 v30, v129, v27
	v_mov_b32_e32 v31, 0
	s_nop 1
	v_mov_b32_dpp v31, v30 quad_perm:[1,0,3,2] row_mask:0xf bank_mask:0xf
	v_fmac_f32_e32 v31, v129, v27
	s_nop 1
	v_add_f32_dpp v27, v31, v31 quad_perm:[2,3,0,1] row_mask:0xf bank_mask:0xf bound_ctrl:1
	s_nop 1
	v_add_f32_dpp v27, v27, v27 row_half_mirror row_mask:0xf bank_mask:0xf bound_ctrl:1
	s_nop 1
	v_mov_b32_dpp v107, v27 row_mirror row_mask:0xf bank_mask:0xf
	s_and_saveexec_b64 s[4:5], vcc
	v_add_f32_e32 v27, v27, v107
	ds_write_b32 v26, v27 offset:4
	s_or_b64 exec, exec, s[4:5]
	v_mul_f32_e32 v30, v129, v28
	v_mov_b32_e32 v31, 0
	v_mov_b32_e32 v27, 0
	s_nop 0
	v_mov_b32_dpp v31, v30 quad_perm:[1,0,3,2] row_mask:0xf bank_mask:0xf
	v_fmac_f32_e32 v31, v129, v28
	v_mov_b32_e32 v30, 0
	s_nop 0
	v_add_f32_dpp v28, v31, v31 quad_perm:[2,3,0,1] row_mask:0xf bank_mask:0xf bound_ctrl:1
	s_nop 1
	v_add_f32_dpp v28, v28, v28 row_half_mirror row_mask:0xf bank_mask:0xf bound_ctrl:1
	s_nop 1
	v_mov_b32_dpp v30, v28 row_mirror row_mask:0xf bank_mask:0xf
	s_and_saveexec_b64 s[4:5], vcc
	v_add_f32_e32 v28, v28, v30
	ds_write_b32 v26, v28 offset:8
	s_or_b64 exec, exec, s[4:5]
	v_mul_f32_e32 v28, v129, v29
	v_mov_b32_e32 v30, 0
	s_nop 1
	v_mov_b32_dpp v30, v28 quad_perm:[1,0,3,2] row_mask:0xf bank_mask:0xf
	v_fmac_f32_e32 v30, v129, v29
	s_nop 1
	v_add_f32_dpp v28, v30, v30 quad_perm:[2,3,0,1] row_mask:0xf bank_mask:0xf bound_ctrl:1
	s_nop 1
	v_add_f32_dpp v28, v28, v28 row_half_mirror row_mask:0xf bank_mask:0xf bound_ctrl:1
	s_nop 1
	v_mov_b32_dpp v27, v28 row_mirror row_mask:0xf bank_mask:0xf
	s_and_saveexec_b64 s[4:5], vcc
	v_add_f32_e32 v27, v28, v27
	ds_write_b32 v26, v27 offset:12
	s_or_b64 exec, exec, s[4:5]
	s_mov_b64 s[4:5], 0
	s_branch .LBB0_28
.Lp_q:
	v_lshrrev_b32_e32 v234, 5, v0
	v_lshlrev_b32_e32 v234, 10, v234
	v_and_b32_e32 v239, 31, v0
	v_lshl_add_u32 v234, v239, 4, v234
	s_and_b32 s13, s2, 7
	s_lshl_b32 s14, s13, 14
	v_add_u32_e32 v239, s14, v234
	global_load_dwordx4 v[164:167], v239, s[28:29]
	s_add_i32 s13, s2, 1
	s_and_b32 s13, s13, 7
	s_lshl_b32 s14, s13, 14
	v_add_u32_e32 v239, s14, v234
	global_load_dwordx4 v[168:171], v239, s[28:29]
	s_add_i32 s13, s2, 2
	s_and_b32 s13, s13, 7
	s_lshl_b32 s14, s13, 14
	v_add_u32_e32 v239, s14, v234
	global_load_dwordx4 v[172:175], v239, s[28:29]
	s_add_i32 s13, s2, 3
	s_and_b32 s13, s13, 7
	s_lshl_b32 s14, s13, 14
	v_add_u32_e32 v239, s14, v234
	global_load_dwordx4 v[176:179], v239, s[28:29]
	s_add_i32 s13, s2, 4
	s_and_b32 s13, s13, 7
	s_lshl_b32 s14, s13, 14
	v_add_u32_e32 v239, s14, v234
	global_load_dwordx4 v[180:183], v239, s[28:29]
	s_add_i32 s13, s2, 5
	s_and_b32 s13, s13, 7
	s_lshl_b32 s14, s13, 14
	v_add_u32_e32 v239, s14, v234
	global_load_dwordx4 v[184:187], v239, s[28:29]
	s_add_i32 s13, s2, 6
	s_and_b32 s13, s13, 7
	s_lshl_b32 s14, s13, 14
	v_add_u32_e32 v239, s14, v234
	global_load_dwordx4 v[188:191], v239, s[28:29]
	s_add_i32 s13, s2, 7
	s_and_b32 s13, s13, 7
	s_lshl_b32 s14, s13, 14
	v_add_u32_e32 v239, s14, v234
	global_load_dwordx4 v[192:195], v239, s[28:29]
	s_waitcnt vmcnt(18)
	v_cvt_pk_bf16_f32 v12, v2, v3
	v_cvt_pk_bf16_f32 v13, v4, v5
	ds_write_b64 v238, v[12:13]
	s_waitcnt vmcnt(17)
	v_cvt_pk_bf16_f32 v6, v132, v133
	v_cvt_pk_bf16_f32 v7, v134, v135
	s_and_b32 s13, s2, 7
	s_mul_i32 s14, s13, 0x1100
	v_add_u32_e32 v239, s14, v58
	ds_write_b64 v239, v[6:7]
	s_waitcnt vmcnt(16)
	v_cvt_pk_bf16_f32 v8, v136, v137
	v_cvt_pk_bf16_f32 v9, v138, v139
	s_add_i32 s13, s2, 1
	s_and_b32 s13, s13, 7
	s_mul_i32 s14, s13, 0x1100
	v_add_u32_e32 v10, s14, v58
	ds_write_b64 v10, v[8:9]
	s_waitcnt vmcnt(15)
	v_cvt_pk_bf16_f32 v6, v140, v141
	v_cvt_pk_bf16_f32 v7, v142, v143
	s_add_i32 s13, s2, 2
	s_and_b32 s13, s13, 7
	s_mul_i32 s14, s13, 0x1100
	v_add_u32_e32 v239, s14, v58
	ds_write_b64 v239, v[6:7]
	s_waitcnt vmcnt(14)
	v_cvt_pk_bf16_f32 v8, v144, v145
	v_cvt_pk_bf16_f32 v9, v146, v147
	s_add_i32 s13, s2, 3
	s_and_b32 s13, s13, 7
	s_mul_i32 s14, s13, 0x1100
	v_add_u32_e32 v10, s14, v58
	ds_write_b64 v10, v[8:9]
	s_waitcnt vmcnt(13)
	v_cvt_pk_bf16_f32 v6, v148, v149
	v_cvt_pk_bf16_f32 v7, v150, v151
	s_add_i32 s13, s2, 4
	s_and_b32 s13, s13, 7
	s_mul_i32 s14, s13, 0x1100
	v_add_u32_e32 v239, s14, v58
	ds_write_b64 v239, v[6:7]
	s_waitcnt vmcnt(12)
	v_cvt_pk_bf16_f32 v8, v152, v153
	v_cvt_pk_bf16_f32 v9, v154, v155
	s_add_i32 s13, s2, 5
	s_and_b32 s13, s13, 7
	s_mul_i32 s14, s13, 0x1100
	v_add_u32_e32 v10, s14, v58
	ds_write_b64 v10, v[8:9]
	s_waitcnt vmcnt(11)
	v_cvt_pk_bf16_f32 v6, v156, v157
	v_cvt_pk_bf16_f32 v7, v158, v159
	s_add_i32 s13, s2, 6
	s_and_b32 s13, s13, 7
	s_mul_i32 s14, s13, 0x1100
	v_add_u32_e32 v239, s14, v58
	ds_write_b64 v239, v[6:7]
	s_waitcnt vmcnt(10)
	v_cvt_pk_bf16_f32 v8, v160, v161
	v_cvt_pk_bf16_f32 v9, v162, v163
	s_add_i32 s13, s2, 7
	s_and_b32 s13, s13, 7
	s_mul_i32 s14, s13, 0x1100
	v_add_u32_e32 v10, s14, v58
	ds_write_b64 v10, v[8:9]
	s_waitcnt lgkmcnt(0)
	s_barrier
	ds_read_b128 v[28:31], v53
	ds_read_b128 v[60:63], v56
	ds_read_b128 v[32:35], v53 offset:64
	ds_read_b128 v[64:67], v56 offset:64
	ds_read_b128 v[36:39], v53 offset:128
	ds_read_b128 v[68:71], v56 offset:128
	ds_read_b128 v[40:43], v53 offset:192
	ds_read_b128 v[72:75], v56 offset:192
	s_waitcnt lgkmcnt(6)
	v_mfma_f32_16x16x32_bf16 v[18:21], v[28:31], v[60:63], 0
	s_waitcnt lgkmcnt(4)
	v_mfma_f32_16x16x32_bf16 v[18:21], v[32:35], v[64:67], v[18:21]
	s_waitcnt lgkmcnt(2)
	v_mfma_f32_16x16x32_bf16 v[18:21], v[36:39], v[68:71], v[18:21]
	s_waitcnt lgkmcnt(0)
	v_mfma_f32_16x16x32_bf16 v[18:21], v[40:43], v[72:75], v[18:21]
	s_nop 7
	v_mul_f32_e32 v18, s44, v18
	v_mul_f32_e32 v19, s44, v19
	v_mul_f32_e32 v20, s44, v20
	v_mul_f32_e32 v21, s44, v21
	v_cvt_pk_bf16_f32 v18, v18, v18
	v_cvt_pk_bf16_f32 v19, v19, v19
	v_cvt_pk_bf16_f32 v20, v20, v20
	v_cvt_pk_bf16_f32 v21, v21, v21
	ds_write_b16 v55, v18
	ds_write_b16 v55, v19 offset:272
	ds_write_b16 v55, v20 offset:544
	ds_write_b16 v55, v21 offset:816
	s_waitcnt vmcnt(7)
	v_cvt_pk_bf16_f32 v6, v164, v165
	v_cvt_pk_bf16_f32 v7, v166, v167
	s_and_b32 s13, s2, 7
	s_mul_i32 s14, s13, 0x1100
	s_add_i32 s14, s14, 34816
	v_add_u32_e32 v239, s14, v58
	ds_write_b64 v239, v[6:7]
	s_waitcnt vmcnt(6)
	v_cvt_pk_bf16_f32 v8, v168, v169
	v_cvt_pk_bf16_f32 v9, v170, v171
	s_add_i32 s13, s2, 1
	s_and_b32 s13, s13, 7
	s_mul_i32 s14, s13, 0x1100
	s_add_i32 s14, s14, 34816
	v_add_u32_e32 v10, s14, v58
	ds_write_b64 v10, v[8:9]
	s_waitcnt vmcnt(5)
	v_cvt_pk_bf16_f32 v6, v172, v173
	v_cvt_pk_bf16_f32 v7, v174, v175
	s_add_i32 s13, s2, 2
	s_and_b32 s13, s13, 7
	s_mul_i32 s14, s13, 0x1100
	s_add_i32 s14, s14, 34816
	v_add_u32_e32 v239, s14, v58
	ds_write_b64 v239, v[6:7]
	s_waitcnt vmcnt(4)
	v_cvt_pk_bf16_f32 v8, v176, v177
	v_cvt_pk_bf16_f32 v9, v178, v179
	s_add_i32 s13, s2, 3
	s_and_b32 s13, s13, 7
	s_mul_i32 s14, s13, 0x1100
	s_add_i32 s14, s14, 34816
	v_add_u32_e32 v10, s14, v58
	ds_write_b64 v10, v[8:9]
	s_waitcnt vmcnt(3)
	v_cvt_pk_bf16_f32 v6, v180, v181
	v_cvt_pk_bf16_f32 v7, v182, v183
	s_add_i32 s13, s2, 4
	s_and_b32 s13, s13, 7
	s_mul_i32 s14, s13, 0x1100
	s_add_i32 s14, s14, 34816
	v_add_u32_e32 v239, s14, v58
	ds_write_b64 v239, v[6:7]
	s_waitcnt vmcnt(2)
	v_cvt_pk_bf16_f32 v8, v184, v185
	v_cvt_pk_bf16_f32 v9, v186, v187
	s_add_i32 s13, s2, 5
	s_and_b32 s13, s13, 7
	s_mul_i32 s14, s13, 0x1100
	s_add_i32 s14, s14, 34816
	v_add_u32_e32 v10, s14, v58
	ds_write_b64 v10, v[8:9]
	s_waitcnt vmcnt(1)
	v_cvt_pk_bf16_f32 v6, v188, v189
	v_cvt_pk_bf16_f32 v7, v190, v191
	s_add_i32 s13, s2, 6
	s_and_b32 s13, s13, 7
	s_mul_i32 s14, s13, 0x1100
	s_add_i32 s14, s14, 34816
	v_add_u32_e32 v239, s14, v58
	ds_write_b64 v239, v[6:7]
	s_waitcnt vmcnt(0)
	v_cvt_pk_bf16_f32 v8, v192, v193
	v_cvt_pk_bf16_f32 v9, v194, v195
	s_add_i32 s13, s2, 7
	s_and_b32 s13, s13, 7
	s_mul_i32 s14, s13, 0x1100
	s_add_i32 s14, s14, 34816
	v_add_u32_e32 v10, s14, v58
	ds_write_b64 v10, v[8:9]
	s_waitcnt lgkmcnt(0)
	s_barrier
	global_load_dwordx4 v[2:5], v236, s[34:35] nt
	global_load_dwordx4 v[6:9], v236, s[34:35] offset:1024 nt
	global_load_dwordx4 v[10:13], v236, s[34:35] offset:2048 nt
	global_load_dwordx4 v[14:17], v236, s[34:35] offset:3072 nt
	ds_read_b128 v[28:31], v54
	ds_read_b128 v[60:63], v57
	ds_read_b128 v[32:35], v54 offset:64
	ds_read_b128 v[64:67], v57 offset:64
	ds_read_b128 v[36:39], v54 offset:128
	ds_read_b128 v[68:71], v57 offset:128
	ds_read_b128 v[40:43], v54 offset:192
	ds_read_b128 v[72:75], v57 offset:192
	s_waitcnt lgkmcnt(6)
	v_mfma_f32_16x16x32_bf16 v[18:21], v[28:31], v[60:63], 0
	s_waitcnt lgkmcnt(4)
	v_mfma_f32_16x16x32_bf16 v[18:21], v[32:35], v[64:67], v[18:21]
	s_waitcnt lgkmcnt(2)
	v_mfma_f32_16x16x32_bf16 v[18:21], v[36:39], v[68:71], v[18:21]
	s_waitcnt lgkmcnt(0)
	v_mfma_f32_16x16x32_bf16 v[18:21], v[40:43], v[72:75], v[18:21]
	s_load_dwordx2 s[4:5], s[0:1], 0x68
	v_lshl_or_b32 v26, v24, 2, s12
	v_mov_b32_e32 v107, 0
	v_ashrrev_i32_e32 v27, 31, v26
	v_lshlrev_b64 v[28:29], 9, v[26:27]
	s_waitcnt lgkmcnt(0)
	v_lshl_add_u64 v[30:31], s[4:5], 0, v[106:107]
	v_lshl_add_u64 v[28:29], v[30:31], 0, v[28:29]
	v_mul_u32_u24_e32 v24, 0x440, v24
	s_mov_b32 s4, 0x19200
	global_store_dword v[28:29], v18, off sc1
	v_add3_u32 v28, v24, v25, s4
	v_mul_f32_e32 v24, v18, v18
	v_cvt_pk_bf16_f32 v27, v18, s0
	v_cvt_pk_bf16_f32 v24, v24, s0
	ds_write_b16 v28, v27
	ds_write_b16 v28, v24 offset:4352
	v_max3_f32 v27, |v18|, 0, |v19|
	v_or_b32_e32 v24, 1, v26
	v_cvt_pk_bf16_f32 v18, v19, s0
	v_ashrrev_i32_e32 v25, 31, v24
	ds_write_b16 v28, v18 offset:272
	v_mul_f32_e32 v18, v19, v19
	v_lshlrev_b64 v[24:25], 9, v[24:25]
	v_cvt_pk_bf16_f32 v18, v18, s0
	v_lshl_add_u64 v[24:25], v[30:31], 0, v[24:25]
	ds_write_b16 v28, v18 offset:4624
	v_or_b32_e32 v18, 2, v26
	global_store_dword v[24:25], v19, off sc1
	v_ashrrev_i32_e32 v19, 31, v18
	v_lshlrev_b64 v[18:19], 9, v[18:19]
	v_lshl_add_u64 v[18:19], v[30:31], 0, v[18:19]
	global_store_dword v[18:19], v20, off sc1
	v_cvt_pk_bf16_f32 v18, v20, s0
	ds_write_b16 v28, v18 offset:544
	v_mul_f32_e32 v18, v20, v20
	v_cvt_pk_bf16_f32 v18, v18, s0
	ds_write_b16 v28, v18 offset:4896
	v_or_b32_e32 v18, 3, v26
	v_ashrrev_i32_e32 v19, 31, v18
	v_lshlrev_b64 v[18:19], 9, v[18:19]
	v_lshl_add_u64 v[18:19], v[30:31], 0, v[18:19]
	global_store_dword v[18:19], v21, off sc1
	v_cvt_pk_bf16_f32 v18, v21, s0
	ds_write_b16 v28, v18 offset:816
	v_mul_f32_e32 v18, v21, v21
	v_cvt_pk_bf16_f32 v18, v18, s0
	v_max3_f32 v20, v27, |v20|, |v21|
	ds_write_b16 v28, v18 offset:5168
	v_mov_b32_e32 v18, v107
	v_mov_b32_e32 v19, v107
	v_cmp_eq_u32_e32 vcc, 0, v126
	v_mov_b32_dpp v18, v20 quad_perm:[1,0,3,2] row_mask:0xf bank_mask:0xf
	v_max_f32_e32 v18, v18, v18
	v_max_f32_e32 v18, v20, v18
	s_nop 1
	v_mov_b32_dpp v19, v18 quad_perm:[2,3,0,1] row_mask:0xf bank_mask:0xf
	v_max_f32_e32 v19, v19, v19
	v_max_f32_e32 v18, v18, v19
	v_mov_b32_e32 v19, v107
	s_nop 1
	v_mov_b32_dpp v19, v18 row_half_mirror row_mask:0xf bank_mask:0xf
	v_max_f32_e32 v19, v19, v19
	v_max_f32_e32 v18, v18, v19
	v_mov_b32_e32 v19, v107
	s_nop 1
	v_mov_b32_dpp v19, v18 row_mirror row_mask:0xf bank_mask:0xf
	v_max_f32_e32 v19, v19, v19
	v_max_f32_e32 v18, v18, v19
	s_nop 0
	v_readlane_b32 s8, v18, 0
	v_readlane_b32 s9, v18, 16
	v_readlane_b32 s10, v18, 32
	v_readlane_b32 s11, v18, 48
	v_and_b32_e32 v18, 0x7fffffff, v129
	s_nop 1
	v_add_f32_dpp v18, v18, |v129| quad_perm:[1,0,3,2] row_mask:0xf bank_mask:0xf bound_ctrl:1
	s_nop 1
	v_add_f32_dpp v18, v18, v18 quad_perm:[2,3,0,1] row_mask:0xf bank_mask:0xf bound_ctrl:1
	s_nop 1
	v_add_f32_dpp v18, v18, v18 row_half_mirror row_mask:0xf bank_mask:0xf bound_ctrl:1
	s_nop 1
	v_mov_b32_dpp v107, v18 row_mirror row_mask:0xf bank_mask:0xf
	s_and_saveexec_b64 s[4:5], vcc
	s_cbranch_execz .LBB0_27
	v_mov_b32_e32 v19, 0x1d800
	v_lshl_or_b32 v20, v128, 6, v19
	v_add_f32_e32 v19, v18, v107
	v_max_f32_e64 v18, s11, s11
	v_max_f32_e64 v21, s10, s10
	v_max_f32_e32 v18, v21, v18
	v_mov_b32_e32 v21, s9
	v_max3_f32 v18, s8, v21, v18
	ds_write_b64 v20, v[18:19]

.LBB0_40:
	s_waitcnt vmcnt(5)
	v_mov_b32_e32 v44, 0
	v_cmp_ne_u32_e64 s[46:47], 0, v17
	v_cmp_ne_u32_e64 s[48:49], 0, v16
	v_cmp_ne_u32_e64 s[50:51], 0, v15
	v_cmp_ne_u32_e64 s[52:53], 0, v14
	v_addc_co_u32_e64 v44, s[54:55], v44, v44, s[46:47]
	v_addc_co_u32_e64 v44, s[54:55], v44, v44, s[48:49]
	v_addc_co_u32_e64 v44, s[54:55], v44, v44, s[50:51]
	v_addc_co_u32_e64 v44, s[54:55], v44, v44, s[52:53]
	v_cmp_ne_u32_e64 s[46:47], 0, v13
	v_cmp_ne_u32_e64 s[48:49], 0, v12
	v_cmp_ne_u32_e64 s[50:51], 0, v11
	v_cmp_ne_u32_e64 s[52:53], 0, v10
	v_addc_co_u32_e64 v44, s[54:55], v44, v44, s[46:47]
	v_addc_co_u32_e64 v44, s[54:55], v44, v44, s[48:49]
	v_addc_co_u32_e64 v44, s[54:55], v44, v44, s[50:51]
	v_addc_co_u32_e64 v44, s[54:55], v44, v44, s[52:53]
	v_cmp_ne_u32_e64 s[46:47], 0, v9
	v_cmp_ne_u32_e64 s[48:49], 0, v8
	v_cmp_ne_u32_e64 s[50:51], 0, v7
	v_cmp_ne_u32_e64 s[52:53], 0, v6
	v_addc_co_u32_e64 v44, s[54:55], v44, v44, s[46:47]
	v_addc_co_u32_e64 v44, s[54:55], v44, v44, s[48:49]
	v_addc_co_u32_e64 v44, s[54:55], v44, v44, s[50:51]
	v_addc_co_u32_e64 v44, s[54:55], v44, v44, s[52:53]
	v_cmp_ne_u32_e64 s[46:47], 0, v5
	v_cmp_ne_u32_e64 s[48:49], 0, v4
	v_cmp_ne_u32_e64 s[50:51], 0, v3
	v_cmp_ne_u32_e64 s[52:53], 0, v2
	v_addc_co_u32_e64 v44, s[54:55], v44, v44, s[46:47]
	v_addc_co_u32_e64 v44, s[54:55], v44, v44, s[48:49]
	v_addc_co_u32_e64 v44, s[54:55], v44, v44, s[50:51]
	v_addc_co_u32_e64 v44, s[54:55], v44, v44, s[52:53]
	v_lshl_or_b32 v46, s2, 3, v128
	v_lshlrev_b32_e32 v46, 7, v46
	v_lshl_add_u32 v46, v126, 1, v46
	global_store_short v46, v44, s[36:37] sc1
	s_endpgm

	.amdhsa_kernel _Z11prep_kernelPKfS0_S0_S0_S0_S0_S0_S0_S0_PKiPDv8_DF16bS4_PfS5_S5_PiPt
		.amdhsa_group_segment_fixed_size 121344
		.amdhsa_private_segment_fixed_size 0
		.amdhsa_kernarg_size 136
		.amdhsa_user_sgpr_count 2
		.amdhsa_user_sgpr_dispatch_ptr 0
		.amdhsa_user_sgpr_queue_ptr 0
		.amdhsa_user_sgpr_kernarg_segment_ptr 1
		.amdhsa_user_sgpr_dispatch_id 0
		.amdhsa_user_sgpr_kernarg_preload_length 0
		.amdhsa_user_sgpr_kernarg_preload_offset 0
		.amdhsa_user_sgpr_private_segment_size 0
		.amdhsa_uses_dynamic_stack 0
		.amdhsa_enable_private_segment 0
		.amdhsa_system_sgpr_workgroup_id_x 1
		.amdhsa_system_sgpr_workgroup_id_y 0
		.amdhsa_system_sgpr_workgroup_id_z 0
		.amdhsa_system_sgpr_workgroup_info 0
		.amdhsa_system_vgpr_workitem_id 0
		.amdhsa_next_free_vgpr 248
		.amdhsa_next_free_sgpr 96
		.amdhsa_accum_offset 248
		.amdhsa_reserve_vcc 1
		.amdhsa_float_round_mode_32 0
		.amdhsa_float_round_mode_16_64 0
		.amdhsa_float_denorm_mode_32 3
		.amdhsa_float_denorm_mode_16_64 3
		.amdhsa_dx10_clamp 1
		.amdhsa_ieee_mode 1
		.amdhsa_fp16_overflow 0
		.amdhsa_tg_split 0
		.amdhsa_exception_fp_ieee_invalid_op 0
		.amdhsa_exception_fp_denorm_src 0
		.amdhsa_exception_fp_ieee_div_zero 0
		.amdhsa_exception_fp_ieee_overflow 0
		.amdhsa_exception_fp_ieee_underflow 0
		.amdhsa_exception_fp_ieee_inexact 0
		.amdhsa_exception_int_div_zero 0
	.end_amdhsa_kernel

amdhsa.kernels:
  - .agpr_count:     0
    .args:
      - .actual_access:  read_only
        .address_space:  global
        .offset:         0
        .size:           8
        .value_kind:     global_buffer
      - .actual_access:  read_only
        .address_space:  global
        .offset:         8
        .size:           8
        .value_kind:     global_buffer
      - .actual_access:  read_only
        .address_space:  global
        .offset:         16
        .size:           8
        .value_kind:     global_buffer
      - .actual_access:  read_only
        .address_space:  global
        .offset:         24
        .size:           8
        .value_kind:     global_buffer
      - .actual_access:  read_only
        .address_space:  global
        .offset:         32
        .size:           8
        .value_kind:     global_buffer
      - .actual_access:  read_only
        .address_space:  global
        .offset:         40
        .size:           8
        .value_kind:     global_buffer
      - .actual_access:  read_only
        .address_space:  global
        .offset:         48
        .size:           8
        .value_kind:     global_buffer
      - .actual_access:  read_only
        .address_space:  global
        .offset:         56
        .size:           8
        .value_kind:     global_buffer
      - .actual_access:  read_only
        .address_space:  global
        .offset:         64
        .size:           8
        .value_kind:     global_buffer
      - .actual_access:  read_only
        .address_space:  global
        .offset:         72
        .size:           8
        .value_kind:     global_buffer
      - .actual_access:  write_only
        .address_space:  global
        .offset:         80
        .size:           8
        .value_kind:     global_buffer
      - .actual_access:  write_only
        .address_space:  global
        .offset:         88
        .size:           8
        .value_kind:     global_buffer
      - .actual_access:  write_only
        .address_space:  global
        .offset:         96
        .size:           8
        .value_kind:     global_buffer
      - .actual_access:  write_only
        .address_space:  global
        .offset:         104
        .size:           8
        .value_kind:     global_buffer
      - .actual_access:  write_only
        .address_space:  global
        .offset:         112
        .size:           8
        .value_kind:     global_buffer
      - .actual_access:  write_only
        .address_space:  global
        .offset:         120
        .size:           8
        .value_kind:     global_buffer
      - .actual_access:  write_only
        .address_space:  global
        .offset:         128
        .size:           8
        .value_kind:     global_buffer
    .group_segment_fixed_size: 121344
    .kernarg_segment_align: 8
    .kernarg_segment_size: 136
    .language:       OpenCL C
    .language_version:
      - 2
      - 0
    .max_flat_workgroup_size: 512
    .name:           _Z11prep_kernelPKfS0_S0_S0_S0_S0_S0_S0_S0_PKiPDv8_DF16bS4_PfS5_S5_PiPt
    .private_segment_fixed_size: 0
    .sgpr_count:     31
    .sgpr_spill_count: 0
    .symbol:         _Z11prep_kernelPKfS0_S0_S0_S0_S0_S0_S0_S0_PKiPDv8_DF16bS4_PfS5_S5_PiPt.kd
    .uniform_work_group_size: 1
    .uses_dynamic_stack: false
    .vgpr_count:     248
    .vgpr_spill_count: 0
    .wavefront_size: 64
  - .agpr_count:     0
    .args:
      - .actual_access:  read_only
        .address_space:  global
        .offset:         0
        .size:           8
        .value_kind:     global_buffer
      - .actual_access:  read_only
        .address_space:  global
        .offset:         8
        .size:           8
        .value_kind:     global_buffer
      - .actual_access:  read_only
        .address_space:  global
        .offset:         16
        .size:           8
        .value_kind:     global_buffer
      - .actual_access:  read_only
        .address_space:  global
        .offset:         24
        .size:           8
        .value_kind:     global_buffer
      - .actual_access:  read_only
        .address_space:  global
        .offset:         32
        .size:           8
        .value_kind:     global_buffer
      - .actual_access:  read_only
        .address_space:  global
        .offset:         40
        .size:           8
        .value_kind:     global_buffer
      - .actual_access:  read_only
        .address_space:  global
        .offset:         48
        .size:           8
        .value_kind:     global_buffer
      - .actual_access:  read_only
        .address_space:  global
        .offset:         56
        .size:           8
        .value_kind:     global_buffer
      - .actual_access:  read_only
        .address_space:  global
        .offset:         64
        .size:           8
        .value_kind:     global_buffer
      - .actual_access:  write_only
        .address_space:  global
        .offset:         72
        .size:           8
        .value_kind:     global_buffer
    .group_segment_fixed_size: 70400
    .kernarg_segment_align: 8
    .kernarg_segment_size: 80
    .language:       OpenCL C
    .language_version:
      - 2
      - 0
    .max_flat_workgroup_size: 512
    .name:           _Z11main_kernelPKDv8_DF16bS1_PKfS3_S3_PKiPKtS3_S3_Pf
    .private_segment_fixed_size: 0
    .sgpr_count:     54
    .sgpr_spill_count: 0
    .symbol:         _Z11main_kernelPKDv8_DF16bS1_PKfS3_S3_PKiPKtS3_S3_Pf.kd
    .uniform_work_group_size: 1
    .uses_dynamic_stack: false
    .vgpr_count:     204
    .vgpr_spill_count: 0
    .wavefront_size: 64
